# speedup vs baseline: 1.0061x; 1.0045x over previous
_ZN12_GLOBAL__N_14k_fcEPKtPKiS1_PKfS5_Pf:
	s_load_dwordx8 s[4:11], s[0:1], 0x0
	s_load_dwordx4 s[12:15], s[0:1], 0x20
	s_and_b32 s3, s2, 7
	s_lshr_b32 s20, s2, 3
	s_lshr_b32 s19, s20, 2
	s_lshl_b32 s3, s3, 3
	s_add_u32 s19, s19, s3
	s_and_b32 s20, s20, 3
	v_lshrrev_b32_e32 v1, 6, v0
	v_and_b32_e32 v12, 63, v0
	v_and_b32_e32 v13, 15, v0
	v_readfirstlane_b32 s16, v1
	v_lshrrev_b32_e32 v14, 4, v12
	s_nop 3
	s_lshr_b32 s17, s16, 2
	s_and_b32 s18, s16, 3
	v_lshrrev_b32_e32 v70, 2, v12
	s_lshl_b32 s90, s19, 8
	s_lshl_b32 s91, s16, 5
	s_add_u32 s90, s90, s91
	v_add_u32_e32 v73, s90, v70
	v_add_u32_e32 v74, 16, v73
	v_lshlrev_b32_e32 v75, 3, v73
	v_lshlrev_b32_e32 v76, 3, v74
	s_waitcnt lgkmcnt(0)
	global_load_dwordx2 v[64:65], v75, s[6:7]
	global_load_dwordx2 v[66:67], v76, s[6:7]
	s_mul_i32 s90, s20, 0x180
	s_mul_i32 s91, s18, 96
	s_add_u32 s90, s90, s91
	v_lshl_add_u32 v15, v14, 2, s90
	v_lshlrev_b32_e32 v15, 2, v15
	global_load_dwordx4 v[16:19], v15, s[10:11] offset:0
	global_load_dwordx4 v[20:23], v15, s[10:11] offset:64
	global_load_dwordx4 v[24:27], v15, s[10:11] offset:128
	global_load_dwordx4 v[28:31], v15, s[10:11] offset:192
	global_load_dwordx4 v[32:35], v15, s[10:11] offset:256
	global_load_dwordx4 v[36:39], v15, s[10:11] offset:320
	v_mul_u32_u24_e32 v77, 0x1800, v13
	v_add_u32_e32 v77, v77, v15
	v_mov_b32_e32 v40, 0
	v_mov_b32_e32 v41, 0
	v_mov_b32_e32 v42, 0
	v_mov_b32_e32 v43, 0
	v_mov_b32_e32 v44, 0
	v_mov_b32_e32 v45, 0
	v_mov_b32_e32 v46, 0
	v_mov_b32_e32 v47, 0
	v_mov_b32_e32 v48, 0
	v_mov_b32_e32 v49, 0
	v_mov_b32_e32 v50, 0
	v_mov_b32_e32 v51, 0
	v_mov_b32_e32 v52, 0
	v_mov_b32_e32 v53, 0
	v_mov_b32_e32 v54, 0
	v_mov_b32_e32 v55, 0
	v_mov_b32_e32 v56, 0
	v_mov_b32_e32 v57, 0
	v_mov_b32_e32 v58, 0
	v_mov_b32_e32 v59, 0
	v_mov_b32_e32 v60, 0
	v_mov_b32_e32 v61, 0
	v_mov_b32_e32 v62, 0
	v_mov_b32_e32 v63, 0
	s_mov_b32 exec_lo, 0xff00ff
	s_mov_b32 exec_hi, 0xff00ff
	global_load_dwordx4 v[40:43], v77, s[12:13] offset:0
	global_load_dwordx4 v[44:47], v77, s[12:13] offset:64
	global_load_dwordx4 v[48:51], v77, s[12:13] offset:128
	global_load_dwordx4 v[52:55], v77, s[12:13] offset:192
	global_load_dwordx4 v[56:59], v77, s[12:13] offset:256
	global_load_dwordx4 v[60:63], v77, s[12:13] offset:320
	s_mov_b64 exec, -1
	v_lshlrev_b32_e32 v15, 6, v13
	v_lshl_add_u32 v15, v14, 4, v15
	v_lshrrev_b32_e32 v78, 3, v13
	v_lshlrev_b32_e32 v78, 5, v78
	v_xor_b32_e32 v15, v15, v78
	s_lshl_b32 s90, s17, 13
	v_add_u32_e32 v1, s90, v15
	v_add_u32_e32 v2, 0x14000, v1
	s_mul_i32 s90, s18, 0x1800
	s_add_u32 s90, s90, 0x4000
	v_add_u32_e32 v3, s90, v15
	v_add_u32_e32 v4, 0x14000, v3
	v_and_b32_e32 v71, 3, v12
	v_lshrrev_b32_e32 v72, 5, v12
	v_lshlrev_b32_e32 v72, 1, v72
	v_xor_b32_e32 v71, v71, v72
	v_lshlrev_b32_e32 v71, 4, v71
	v_lshl_add_u32 v11, v70, 6, v71
	s_mul_i32 s90, s20, 0x180
	s_mul_i32 s91, s16, 48
	s_add_u32 s90, s90, s91
	s_lshl_b32 s90, s90, 6
	s_add_u32 s28, s8, s90
	s_addc_u32 s29, s9, 0
	s_add_u32 s30, s28, 0x18000
	s_addc_u32 s31, s29, 0
	s_add_u32 s32, s28, 0x400
	s_addc_u32 s33, s29, 0
	s_add_u32 s34, s32, 0x18000
	s_addc_u32 s35, s33, 0
	s_add_u32 s36, s28, 0x800
	s_addc_u32 s37, s29, 0
	s_add_u32 s38, s36, 0x18000
	s_addc_u32 s39, s37, 0
	s_mov_b64 s[24:25], s[4:5]
	s_add_u32 s26, s4, 0x40
	s_addc_u32 s27, s5, 0
	s_add_u32 s96, s4, 0x1000000
	s_addc_u32 s97, s5, 0
	s_lshl_b32 s22, s16, 11
	s_mul_i32 s23, s16, 0xc00
	s_add_u32 s23, s23, 0x4000
	s_mov_b32 s21, 0
	s_lshr_b32 s92, s19, 1
	s_lshl_b32 s92, s92, 9
	s_movk_i32 s93, 0x1ff
	s_movk_i32 s94, 0x200
	v_lshl_add_u32 v5, v73, 10, v71
	v_lshl_add_u32 v6, v74, 10, v71
	s_add_u32 s24, s24, 0x1000000
	s_addc_u32 s25, s25, 0
	s_add_u32 s26, s26, 0x1000000
	s_addc_u32 s27, s27, 0
	s_add_u32 s28, s28, 0x180000
	s_addc_u32 s29, s29, 0
	s_add_u32 s30, s30, 0x180000
	s_addc_u32 s31, s31, 0
	s_add_u32 s32, s32, 0x180000
	s_addc_u32 s33, s33, 0
	s_add_u32 s34, s34, 0x180000
	s_addc_u32 s35, s35, 0
	s_add_u32 s36, s36, 0x180000
	s_addc_u32 s37, s37, 0
	s_add_u32 s38, s38, 0x180000
	s_addc_u32 s39, s39, 0
	s_cmp_lg_u32 s17, 0
	s_cbranch_scc1 .Lfc_h1_entry
	s_add_u32 m0, s22, 0x0
	s_nop 0
	global_load_lds_dwordx4 v5, s[24:25]
	s_add_u32 m0, s22, 0x400
	s_nop 0
	global_load_lds_dwordx4 v6, s[24:25]
	s_add_u32 m0, s23, 0x0
	s_nop 0
	global_load_lds_dwordx4 v11, s[28:29]
	s_add_u32 m0, s23, 0x400
	s_nop 0
	global_load_lds_dwordx4 v11, s[32:33]
	s_add_u32 m0, s23, 0x800
	s_nop 0
	global_load_lds_dwordx4 v11, s[36:37]
	s_add_u32 s24, s24, 0x80
	s_addc_u32 s25, s25, 0
	s_add_u32 s28, s28, 0x30000
	s_addc_u32 s29, s29, 0
	s_add_u32 s32, s32, 0x30000
	s_addc_u32 s33, s33, 0
	s_add_u32 s36, s36, 0x30000
	s_addc_u32 s37, s37, 0
	s_add_u32 m0, s22, 0xa000
	s_nop 0
	global_load_lds_dwordx4 v5, s[26:27]
	s_add_u32 m0, s22, 0xa400
	s_nop 0
	global_load_lds_dwordx4 v6, s[26:27]
	s_add_u32 m0, s23, 0xa000
	s_nop 0
	global_load_lds_dwordx4 v11, s[30:31]
	s_add_u32 m0, s23, 0xa400
	s_nop 0
	global_load_lds_dwordx4 v11, s[34:35]
	s_add_u32 m0, s23, 0xa800
	s_nop 0
	global_load_lds_dwordx4 v11, s[38:39]
	s_add_u32 s26, s26, 0x80
	s_addc_u32 s27, s27, 0
	s_add_u32 s30, s30, 0x30000
	s_addc_u32 s31, s31, 0
	s_add_u32 s34, s34, 0x30000
	s_addc_u32 s35, s35, 0
	s_add_u32 s38, s38, 0x30000
	s_addc_u32 s39, s39, 0
	s_waitcnt vmcnt(10)
	v_med3_i32 v64, v64, 0, s93
	v_med3_i32 v65, v65, 1, s94
	v_med3_i32 v66, v66, 0, s93
	v_med3_i32 v67, v67, 1, s94
	v_add_u32_e32 v64, s92, v64
	v_add_u32_e32 v66, s92, v66
	v_add_u32_e32 v65, s92, v65
	v_add_u32_e32 v67, s92, v67
	v_add_u32_e32 v65, -1, v65
	v_add_u32_e32 v67, -1, v67
	v_lshl_add_u32 v7, v64, 10, v71
	v_lshl_add_u32 v8, v66, 10, v71
	v_lshl_add_u32 v9, v65, 10, v71
	v_lshl_add_u32 v10, v67, 10, v71
	v_cvt_pk_f16_f32 v12, v40, v41
	v_cvt_pk_f16_f32 v13, v42, v43
	v_cvt_pk_f16_f32 v14, v44, v45
	v_cvt_pk_f16_f32 v15, v46, v47
	v_cvt_pk_f16_f32 v56, v56, v57
	v_cvt_pk_f16_f32 v57, v58, v59
	v_cvt_pk_f16_f32 v58, v60, v61
	v_cvt_pk_f16_f32 v59, v62, v63
	v_cvt_pk_f16_f32 v60, v48, v49
	v_cvt_pk_f16_f32 v61, v50, v51
	v_cvt_pk_f16_f32 v62, v52, v53
	v_cvt_pk_f16_f32 v63, v54, v55
	v_mov_b32_e32 v64, v16
	v_mov_b32_e32 v65, v17
	v_mov_b32_e32 v66, v18
	v_mov_b32_e32 v67, v19
	v_mov_b32_e32 v68, v20
	v_mov_b32_e32 v69, v21
	v_mov_b32_e32 v70, v22
	v_mov_b32_e32 v71, v23
	v_mov_b32_e32 v72, v24
	v_mov_b32_e32 v73, v25
	v_mov_b32_e32 v74, v26
	v_mov_b32_e32 v75, v27
	v_mov_b32_e32 v76, v28
	v_mov_b32_e32 v77, v29
	v_mov_b32_e32 v78, v30
	v_mov_b32_e32 v79, v31
	v_mov_b32_e32 v80, v32
	v_mov_b32_e32 v81, v33
	v_mov_b32_e32 v82, v34
	v_mov_b32_e32 v83, v35
	v_mov_b32_e32 v84, v36
	v_mov_b32_e32 v85, v37
	v_mov_b32_e32 v86, v38
	v_mov_b32_e32 v87, v39
	v_mov_b32_e32 v88, v16
	v_mov_b32_e32 v89, v17
	v_mov_b32_e32 v90, v18
	v_mov_b32_e32 v91, v19
	v_mov_b32_e32 v92, v20
	v_mov_b32_e32 v93, v21
	v_mov_b32_e32 v94, v22
	v_mov_b32_e32 v95, v23
	v_mov_b32_e32 v96, v24
	v_mov_b32_e32 v97, v25
	v_mov_b32_e32 v98, v26
	v_mov_b32_e32 v99, v27
	v_mov_b32_e32 v100, v28
	v_mov_b32_e32 v101, v29
	v_mov_b32_e32 v102, v30
	v_mov_b32_e32 v103, v31
	v_mov_b32_e32 v104, v32
	v_mov_b32_e32 v105, v33
	v_mov_b32_e32 v106, v34
	v_mov_b32_e32 v107, v35
	v_mov_b32_e32 v108, v36
	v_mov_b32_e32 v109, v37
	v_mov_b32_e32 v110, v38
	v_mov_b32_e32 v111, v39
	v_mov_b32_e32 v112, v16
	v_mov_b32_e32 v113, v17
	v_mov_b32_e32 v114, v18
	v_mov_b32_e32 v115, v19
	v_mov_b32_e32 v116, v20
	v_mov_b32_e32 v117, v21
	v_mov_b32_e32 v118, v22
	v_mov_b32_e32 v119, v23
	v_mov_b32_e32 v120, v24
	v_mov_b32_e32 v121, v25
	v_mov_b32_e32 v122, v26
	v_mov_b32_e32 v123, v27
	v_mov_b32_e32 v124, v28
	v_mov_b32_e32 v125, v29
	v_mov_b32_e32 v126, v30
	v_mov_b32_e32 v127, v31
	v_mov_b32_e32 v128, v32
	v_mov_b32_e32 v129, v33
	v_mov_b32_e32 v130, v34
	v_mov_b32_e32 v131, v35
	v_mov_b32_e32 v132, v36
	v_mov_b32_e32 v133, v37
	v_mov_b32_e32 v134, v38
	v_mov_b32_e32 v135, v39
	v_mov_b32_e32 v136, v16
	v_mov_b32_e32 v137, v17
	v_mov_b32_e32 v138, v18
	v_mov_b32_e32 v139, v19
	v_mov_b32_e32 v140, v20
	v_mov_b32_e32 v141, v21
	v_mov_b32_e32 v142, v22
	v_mov_b32_e32 v143, v23
	v_mov_b32_e32 v144, v24
	v_mov_b32_e32 v145, v25
	v_mov_b32_e32 v146, v26
	v_mov_b32_e32 v147, v27
	v_mov_b32_e32 v148, v28
	v_mov_b32_e32 v149, v29
	v_mov_b32_e32 v150, v30
	v_mov_b32_e32 v151, v31
	v_mov_b32_e32 v152, v32
	v_mov_b32_e32 v153, v33
	v_mov_b32_e32 v154, v34
	v_mov_b32_e32 v155, v35
	v_mov_b32_e32 v156, v36
	v_mov_b32_e32 v157, v37
	v_mov_b32_e32 v158, v38
	v_mov_b32_e32 v159, v39
	v_mov_b32_e32 v160, v16
	v_mov_b32_e32 v161, v17
	v_mov_b32_e32 v162, v18
	v_mov_b32_e32 v163, v19
	v_mov_b32_e32 v164, v20
	v_mov_b32_e32 v165, v21
	v_mov_b32_e32 v166, v22
	v_mov_b32_e32 v167, v23
	v_mov_b32_e32 v168, v24
	v_mov_b32_e32 v169, v25
	v_mov_b32_e32 v170, v26
	v_mov_b32_e32 v171, v27
	v_mov_b32_e32 v172, v28
	v_mov_b32_e32 v173, v29
	v_mov_b32_e32 v174, v30
	v_mov_b32_e32 v175, v31
	v_mov_b32_e32 v176, v32
	v_mov_b32_e32 v177, v33
	v_mov_b32_e32 v178, v34
	v_mov_b32_e32 v179, v35
	v_mov_b32_e32 v180, v36
	v_mov_b32_e32 v181, v37
	v_mov_b32_e32 v182, v38
	v_mov_b32_e32 v183, v39
	v_mov_b32_e32 v184, v16
	v_mov_b32_e32 v185, v17
	v_mov_b32_e32 v186, v18
	v_mov_b32_e32 v187, v19
	v_mov_b32_e32 v188, v20
	v_mov_b32_e32 v189, v21
	v_mov_b32_e32 v190, v22
	v_mov_b32_e32 v191, v23
	v_mov_b32_e32 v192, v24
	v_mov_b32_e32 v193, v25
	v_mov_b32_e32 v194, v26
	v_mov_b32_e32 v195, v27
	v_mov_b32_e32 v196, v28
	v_mov_b32_e32 v197, v29
	v_mov_b32_e32 v198, v30
	v_mov_b32_e32 v199, v31
	v_mov_b32_e32 v200, v32
	v_mov_b32_e32 v201, v33
	v_mov_b32_e32 v202, v34
	v_mov_b32_e32 v203, v35
	v_mov_b32_e32 v204, v36
	v_mov_b32_e32 v205, v37
	v_mov_b32_e32 v206, v38
	v_mov_b32_e32 v207, v39
	v_mov_b32_e32 v208, v16
	v_mov_b32_e32 v209, v17
	v_mov_b32_e32 v210, v18
	v_mov_b32_e32 v211, v19
	v_mov_b32_e32 v212, v20
	v_mov_b32_e32 v213, v21
	v_mov_b32_e32 v214, v22
	v_mov_b32_e32 v215, v23
	v_mov_b32_e32 v216, v24
	v_mov_b32_e32 v217, v25
	v_mov_b32_e32 v218, v26
	v_mov_b32_e32 v219, v27
	v_mov_b32_e32 v220, v28
	v_mov_b32_e32 v221, v29
	v_mov_b32_e32 v222, v30
	v_mov_b32_e32 v223, v31
	v_mov_b32_e32 v224, v32
	v_mov_b32_e32 v225, v33
	v_mov_b32_e32 v226, v34
	v_mov_b32_e32 v227, v35
	v_mov_b32_e32 v228, v36
	v_mov_b32_e32 v229, v37
	v_mov_b32_e32 v230, v38
	v_mov_b32_e32 v231, v39
	v_mov_b32_e32 v232, v16
	v_mov_b32_e32 v233, v17
	v_mov_b32_e32 v234, v18
	v_mov_b32_e32 v235, v19
	v_mov_b32_e32 v236, v20
	v_mov_b32_e32 v237, v21
	v_mov_b32_e32 v238, v22
	v_mov_b32_e32 v239, v23
	v_mov_b32_e32 v240, v24
	v_mov_b32_e32 v241, v25
	v_mov_b32_e32 v242, v26
	v_mov_b32_e32 v243, v27
	v_mov_b32_e32 v244, v28
	v_mov_b32_e32 v245, v29
	v_mov_b32_e32 v246, v30
	v_mov_b32_e32 v247, v31
	v_mov_b32_e32 v248, v32
	v_mov_b32_e32 v249, v33
	v_mov_b32_e32 v250, v34
	v_mov_b32_e32 v251, v35
	v_mov_b32_e32 v252, v36
	v_mov_b32_e32 v253, v37
	v_mov_b32_e32 v254, v38
	v_mov_b32_e32 v255, v39
	s_waitcnt vmcnt(5)
	s_barrier
.Lfc_h0_loop:
	ds_read_b128 v[16:19], v3 offset:0
	ds_read_b128 v[20:23], v3 offset:1024
	ds_read_b128 v[24:27], v3 offset:2048
	ds_read_b128 v[28:31], v3 offset:3072
	ds_read_b128 v[32:35], v3 offset:4096
	ds_read_b128 v[36:39], v3 offset:5120
	ds_read_b128 v[40:43], v1 offset:0
	ds_read_b128 v[44:47], v1 offset:1024
	ds_read_b128 v[48:51], v1 offset:2048
	ds_read_b128 v[52:55], v1 offset:3072
	s_add_u32 m0, s22, 0x14000
	s_nop 0
	global_load_lds_dwordx4 v5, s[24:25]
	s_add_u32 m0, s22, 0x14400
	s_nop 0
	global_load_lds_dwordx4 v6, s[24:25]
	s_add_u32 m0, s23, 0x14000
	s_nop 0
	global_load_lds_dwordx4 v11, s[28:29]
	s_add_u32 m0, s23, 0x14400
	s_nop 0
	global_load_lds_dwordx4 v11, s[32:33]
	s_add_u32 m0, s23, 0x14800
	s_nop 0
	global_load_lds_dwordx4 v11, s[36:37]
	s_add_u32 s24, s24, 0x80
	s_addc_u32 s25, s25, 0
	s_add_u32 s28, s28, 0x30000
	s_addc_u32 s29, s29, 0
	s_add_u32 s32, s32, 0x30000
	s_addc_u32 s33, s33, 0
	s_add_u32 s36, s36, 0x30000
	s_addc_u32 s37, s37, 0
	s_barrier
	s_waitcnt lgkmcnt(0)
	v_mfma_f32_16x16x32_f16 v[64:67], v[16:19], v[40:43], v[64:67]
	v_mfma_f32_16x16x32_f16 v[68:71], v[20:23], v[40:43], v[68:71]
	v_mfma_f32_16x16x32_f16 v[72:75], v[24:27], v[40:43], v[72:75]
	v_mfma_f32_16x16x32_f16 v[76:79], v[28:31], v[40:43], v[76:79]
	v_mfma_f32_16x16x32_f16 v[80:83], v[32:35], v[40:43], v[80:83]
	v_mfma_f32_16x16x32_f16 v[84:87], v[36:39], v[40:43], v[84:87]
	v_mfma_f32_16x16x32_f16 v[88:91], v[16:19], v[44:47], v[88:91]
	ds_read_b128 v[40:43], v1 offset:4096
	v_mfma_f32_16x16x32_f16 v[92:95], v[20:23], v[44:47], v[92:95]
	v_mfma_f32_16x16x32_f16 v[96:99], v[24:27], v[44:47], v[96:99]
	v_mfma_f32_16x16x32_f16 v[100:103], v[28:31], v[44:47], v[100:103]
	v_mfma_f32_16x16x32_f16 v[104:107], v[32:35], v[44:47], v[104:107]
	v_mfma_f32_16x16x32_f16 v[108:111], v[36:39], v[44:47], v[108:111]
	v_mfma_f32_16x16x32_f16 v[112:115], v[16:19], v[48:51], v[112:115]
	ds_read_b128 v[44:47], v1 offset:5120
	v_mfma_f32_16x16x32_f16 v[116:119], v[20:23], v[48:51], v[116:119]
	v_mfma_f32_16x16x32_f16 v[120:123], v[24:27], v[48:51], v[120:123]
	v_mfma_f32_16x16x32_f16 v[124:127], v[28:31], v[48:51], v[124:127]
	v_mfma_f32_16x16x32_f16 v[128:131], v[32:35], v[48:51], v[128:131]
	v_mfma_f32_16x16x32_f16 v[132:135], v[36:39], v[48:51], v[132:135]
	v_mfma_f32_16x16x32_f16 v[136:139], v[16:19], v[52:55], v[136:139]
	ds_read_b128 v[48:51], v1 offset:6144
	v_mfma_f32_16x16x32_f16 v[140:143], v[20:23], v[52:55], v[140:143]
	v_mfma_f32_16x16x32_f16 v[144:147], v[24:27], v[52:55], v[144:147]
	v_mfma_f32_16x16x32_f16 v[148:151], v[28:31], v[52:55], v[148:151]
	v_mfma_f32_16x16x32_f16 v[152:155], v[32:35], v[52:55], v[152:155]
	v_mfma_f32_16x16x32_f16 v[156:159], v[36:39], v[52:55], v[156:159]
	s_waitcnt lgkmcnt(2)
	v_mfma_f32_16x16x32_f16 v[160:163], v[16:19], v[40:43], v[160:163]
	ds_read_b128 v[52:55], v1 offset:7168
	v_mfma_f32_16x16x32_f16 v[164:167], v[20:23], v[40:43], v[164:167]
	v_mfma_f32_16x16x32_f16 v[168:171], v[24:27], v[40:43], v[168:171]
	v_mfma_f32_16x16x32_f16 v[172:175], v[28:31], v[40:43], v[172:175]
	v_mfma_f32_16x16x32_f16 v[176:179], v[32:35], v[40:43], v[176:179]
	v_mfma_f32_16x16x32_f16 v[180:183], v[36:39], v[40:43], v[180:183]
	s_waitcnt lgkmcnt(2)
	v_mfma_f32_16x16x32_f16 v[184:187], v[16:19], v[44:47], v[184:187]
	v_mfma_f32_16x16x32_f16 v[188:191], v[20:23], v[44:47], v[188:191]
	v_mfma_f32_16x16x32_f16 v[192:195], v[24:27], v[44:47], v[192:195]
	v_mfma_f32_16x16x32_f16 v[196:199], v[28:31], v[44:47], v[196:199]
	v_mfma_f32_16x16x32_f16 v[200:203], v[32:35], v[44:47], v[200:203]
	v_mfma_f32_16x16x32_f16 v[204:207], v[36:39], v[44:47], v[204:207]
	s_cmp_eq_u32 s21, 11
	s_cbranch_scc1 .Lfc_w0_1
	s_waitcnt vmcnt(5)
	s_branch .Lfc_w1_1

.Lfc_w1_1:
	s_waitcnt lgkmcnt(1)
	v_mfma_f32_16x16x32_f16 v[208:211], v[16:19], v[48:51], v[208:211]
	v_mfma_f32_16x16x32_f16 v[212:215], v[20:23], v[48:51], v[212:215]
	v_mfma_f32_16x16x32_f16 v[216:219], v[24:27], v[48:51], v[216:219]
	v_mfma_f32_16x16x32_f16 v[220:223], v[28:31], v[48:51], v[220:223]
	v_mfma_f32_16x16x32_f16 v[224:227], v[32:35], v[48:51], v[224:227]
	v_mfma_f32_16x16x32_f16 v[228:231], v[36:39], v[48:51], v[228:231]
	s_waitcnt lgkmcnt(0)
	v_mfma_f32_16x16x32_f16 v[232:235], v[16:19], v[52:55], v[232:235]
	v_mfma_f32_16x16x32_f16 v[236:239], v[20:23], v[52:55], v[236:239]
	v_mfma_f32_16x16x32_f16 v[240:243], v[24:27], v[52:55], v[240:243]
	v_mfma_f32_16x16x32_f16 v[244:247], v[28:31], v[52:55], v[244:247]
	v_mfma_f32_16x16x32_f16 v[248:251], v[32:35], v[52:55], v[248:251]
	v_mfma_f32_16x16x32_f16 v[252:255], v[36:39], v[52:55], v[252:255]
	s_barrier
	ds_read_b128 v[16:19], v3 offset:40960
	ds_read_b128 v[20:23], v3 offset:41984
	ds_read_b128 v[24:27], v3 offset:43008
	ds_read_b128 v[28:31], v3 offset:44032
	ds_read_b128 v[32:35], v3 offset:45056
	ds_read_b128 v[36:39], v3 offset:46080
	ds_read_b128 v[40:43], v1 offset:40960
	ds_read_b128 v[44:47], v1 offset:41984
	ds_read_b128 v[48:51], v1 offset:43008
	ds_read_b128 v[52:55], v1 offset:44032
	s_add_u32 m0, s22, 0x1e000
	s_nop 0
	global_load_lds_dwordx4 v5, s[26:27]
	s_add_u32 m0, s22, 0x1e400
	s_nop 0
	global_load_lds_dwordx4 v6, s[26:27]
	s_add_u32 m0, s23, 0x1e000
	s_nop 0
	global_load_lds_dwordx4 v11, s[30:31]
	s_add_u32 m0, s23, 0x1e400
	s_nop 0
	global_load_lds_dwordx4 v11, s[34:35]
	s_add_u32 m0, s23, 0x1e800
	s_nop 0
	global_load_lds_dwordx4 v11, s[38:39]
	s_add_u32 s26, s26, 0x80
	s_addc_u32 s27, s27, 0
	s_add_u32 s30, s30, 0x30000
	s_addc_u32 s31, s31, 0
	s_add_u32 s34, s34, 0x30000
	s_addc_u32 s35, s35, 0
	s_add_u32 s38, s38, 0x30000
	s_addc_u32 s39, s39, 0
	s_cmp_eq_u32 s21, 3
	s_cbranch_scc1 .Lfc_sw_2
	s_cmp_eq_u32 s21, 7
	s_cbranch_scc0 .Lfc_swd_2
	s_add_u32 s28, s28, 0x180000
	s_addc_u32 s29, s29, 0
	s_add_u32 s30, s30, 0x180000
	s_addc_u32 s31, s31, 0
	s_add_u32 s32, s32, 0x180000
	s_addc_u32 s33, s33, 0
	s_add_u32 s34, s34, 0x180000
	s_addc_u32 s35, s35, 0
	s_add_u32 s36, s36, 0x180000
	s_addc_u32 s37, s37, 0
	s_add_u32 s38, s38, 0x180000
	s_addc_u32 s39, s39, 0
	s_branch .Lfc_sw2_2

.Lfc_sw2_2:
	s_mov_b64 s[24:25], s[4:5]
	s_add_u32 s26, s4, 0x40
	s_addc_u32 s27, s5, 0
	v_mov_b32_e32 v5, v7
	v_mov_b32_e32 v6, v8
	v_mov_b32_e32 v7, v9
	v_mov_b32_e32 v8, v10
.Lfc_swd_2:
	s_barrier
	s_waitcnt lgkmcnt(0)
	v_mfma_f32_16x16x32_f16 v[64:67], v[16:19], v[40:43], v[64:67]
	v_mfma_f32_16x16x32_f16 v[68:71], v[20:23], v[40:43], v[68:71]
	v_mfma_f32_16x16x32_f16 v[72:75], v[24:27], v[40:43], v[72:75]
	v_mfma_f32_16x16x32_f16 v[76:79], v[28:31], v[40:43], v[76:79]
	v_mfma_f32_16x16x32_f16 v[80:83], v[32:35], v[40:43], v[80:83]
	v_mfma_f32_16x16x32_f16 v[84:87], v[36:39], v[40:43], v[84:87]
	v_mfma_f32_16x16x32_f16 v[88:91], v[16:19], v[44:47], v[88:91]
	ds_read_b128 v[40:43], v1 offset:45056
	v_mfma_f32_16x16x32_f16 v[92:95], v[20:23], v[44:47], v[92:95]
	v_mfma_f32_16x16x32_f16 v[96:99], v[24:27], v[44:47], v[96:99]
	v_mfma_f32_16x16x32_f16 v[100:103], v[28:31], v[44:47], v[100:103]
	v_mfma_f32_16x16x32_f16 v[104:107], v[32:35], v[44:47], v[104:107]
	v_mfma_f32_16x16x32_f16 v[108:111], v[36:39], v[44:47], v[108:111]
	v_mfma_f32_16x16x32_f16 v[112:115], v[16:19], v[48:51], v[112:115]
	ds_read_b128 v[44:47], v1 offset:46080
	v_mfma_f32_16x16x32_f16 v[116:119], v[20:23], v[48:51], v[116:119]
	v_mfma_f32_16x16x32_f16 v[120:123], v[24:27], v[48:51], v[120:123]
	v_mfma_f32_16x16x32_f16 v[124:127], v[28:31], v[48:51], v[124:127]
	v_mfma_f32_16x16x32_f16 v[128:131], v[32:35], v[48:51], v[128:131]
	v_mfma_f32_16x16x32_f16 v[132:135], v[36:39], v[48:51], v[132:135]
	v_mfma_f32_16x16x32_f16 v[136:139], v[16:19], v[52:55], v[136:139]
	ds_read_b128 v[48:51], v1 offset:47104
	v_mfma_f32_16x16x32_f16 v[140:143], v[20:23], v[52:55], v[140:143]
	v_mfma_f32_16x16x32_f16 v[144:147], v[24:27], v[52:55], v[144:147]
	v_mfma_f32_16x16x32_f16 v[148:151], v[28:31], v[52:55], v[148:151]
	v_mfma_f32_16x16x32_f16 v[152:155], v[32:35], v[52:55], v[152:155]
	v_mfma_f32_16x16x32_f16 v[156:159], v[36:39], v[52:55], v[156:159]
	s_waitcnt lgkmcnt(2)
	v_mfma_f32_16x16x32_f16 v[160:163], v[16:19], v[40:43], v[160:163]
	ds_read_b128 v[52:55], v1 offset:48128
	v_mfma_f32_16x16x32_f16 v[164:167], v[20:23], v[40:43], v[164:167]
	v_mfma_f32_16x16x32_f16 v[168:171], v[24:27], v[40:43], v[168:171]
	v_mfma_f32_16x16x32_f16 v[172:175], v[28:31], v[40:43], v[172:175]
	v_mfma_f32_16x16x32_f16 v[176:179], v[32:35], v[40:43], v[176:179]
	v_mfma_f32_16x16x32_f16 v[180:183], v[36:39], v[40:43], v[180:183]
	s_waitcnt lgkmcnt(2)
	v_mfma_f32_16x16x32_f16 v[184:187], v[16:19], v[44:47], v[184:187]
	v_mfma_f32_16x16x32_f16 v[188:191], v[20:23], v[44:47], v[188:191]
	v_mfma_f32_16x16x32_f16 v[192:195], v[24:27], v[44:47], v[192:195]
	v_mfma_f32_16x16x32_f16 v[196:199], v[28:31], v[44:47], v[196:199]
	v_mfma_f32_16x16x32_f16 v[200:203], v[32:35], v[44:47], v[200:203]
	v_mfma_f32_16x16x32_f16 v[204:207], v[36:39], v[44:47], v[204:207]
	s_cmp_eq_u32 s21, 11
	s_cbranch_scc1 .Lfc_w0_3
	s_waitcnt vmcnt(5)
	s_branch .Lfc_w1_3

.Lfc_h1_entry:
	s_setprio 1
	s_add_u32 m0, s22, 0x0
	s_nop 0
	global_load_lds_dwordx4 v5, s[24:25]
	s_add_u32 m0, s22, 0x400
	s_nop 0
	global_load_lds_dwordx4 v6, s[24:25]
	s_add_u32 m0, s23, 0x0
	s_nop 0
	global_load_lds_dwordx4 v11, s[28:29]
	s_add_u32 m0, s23, 0x400
	s_nop 0
	global_load_lds_dwordx4 v11, s[32:33]
	s_add_u32 m0, s23, 0x800
	s_nop 0
	global_load_lds_dwordx4 v11, s[36:37]
	s_add_u32 s24, s24, 0x80
	s_addc_u32 s25, s25, 0
	s_add_u32 s28, s28, 0x30000
	s_addc_u32 s29, s29, 0
	s_add_u32 s32, s32, 0x30000
	s_addc_u32 s33, s33, 0
	s_add_u32 s36, s36, 0x30000
	s_addc_u32 s37, s37, 0
	s_add_u32 m0, s22, 0xa000
	s_nop 0
	global_load_lds_dwordx4 v5, s[26:27]
	s_add_u32 m0, s22, 0xa400
	s_nop 0
	global_load_lds_dwordx4 v6, s[26:27]
	s_add_u32 m0, s23, 0xa000
	s_nop 0
	global_load_lds_dwordx4 v11, s[30:31]
	s_add_u32 m0, s23, 0xa400
	s_nop 0
	global_load_lds_dwordx4 v11, s[34:35]
	s_add_u32 m0, s23, 0xa800
	s_nop 0
	global_load_lds_dwordx4 v11, s[38:39]
	s_add_u32 s26, s26, 0x80
	s_addc_u32 s27, s27, 0
	s_add_u32 s30, s30, 0x30000
	s_addc_u32 s31, s31, 0
	s_add_u32 s34, s34, 0x30000
	s_addc_u32 s35, s35, 0
	s_add_u32 s38, s38, 0x30000
	s_addc_u32 s39, s39, 0
	s_add_u32 m0, s22, 0x14000
	s_nop 0
	global_load_lds_dwordx4 v5, s[24:25]
	s_add_u32 m0, s22, 0x14400
	s_nop 0
	global_load_lds_dwordx4 v6, s[24:25]
	s_add_u32 m0, s23, 0x14000
	s_nop 0
	global_load_lds_dwordx4 v11, s[28:29]
	s_add_u32 m0, s23, 0x14400
	s_nop 0
	global_load_lds_dwordx4 v11, s[32:33]
	s_add_u32 m0, s23, 0x14800
	s_nop 0
	global_load_lds_dwordx4 v11, s[36:37]
	s_add_u32 s24, s24, 0x80
	s_addc_u32 s25, s25, 0
	s_add_u32 s28, s28, 0x30000
	s_addc_u32 s29, s29, 0
	s_add_u32 s32, s32, 0x30000
	s_addc_u32 s33, s33, 0
	s_add_u32 s36, s36, 0x30000
	s_addc_u32 s37, s37, 0
	s_waitcnt vmcnt(15)
	v_med3_i32 v64, v64, 0, s93
	v_med3_i32 v65, v65, 1, s94
	v_med3_i32 v66, v66, 0, s93
	v_med3_i32 v67, v67, 1, s94
	v_add_u32_e32 v64, s92, v64
	v_add_u32_e32 v66, s92, v66
	v_add_u32_e32 v65, s92, v65
	v_add_u32_e32 v67, s92, v67
	v_add_u32_e32 v65, -1, v65
	v_add_u32_e32 v67, -1, v67
	v_lshl_add_u32 v7, v64, 10, v71
	v_lshl_add_u32 v8, v66, 10, v71
	v_lshl_add_u32 v9, v65, 10, v71
	v_lshl_add_u32 v10, v67, 10, v71
	v_cvt_pk_f16_f32 v12, v40, v41
	v_cvt_pk_f16_f32 v13, v42, v43
	v_cvt_pk_f16_f32 v14, v44, v45
	v_cvt_pk_f16_f32 v15, v46, v47
	v_cvt_pk_f16_f32 v56, v56, v57
	v_cvt_pk_f16_f32 v57, v58, v59
	v_cvt_pk_f16_f32 v58, v60, v61
	v_cvt_pk_f16_f32 v59, v62, v63
	v_cvt_pk_f16_f32 v60, v48, v49
	v_cvt_pk_f16_f32 v61, v50, v51
	v_cvt_pk_f16_f32 v62, v52, v53
	v_cvt_pk_f16_f32 v63, v54, v55
	v_mov_b32_e32 v64, v16
	v_mov_b32_e32 v65, v17
	v_mov_b32_e32 v66, v18
	v_mov_b32_e32 v67, v19
	v_mov_b32_e32 v68, v20
	v_mov_b32_e32 v69, v21
	v_mov_b32_e32 v70, v22
	v_mov_b32_e32 v71, v23
	v_mov_b32_e32 v72, v24
	v_mov_b32_e32 v73, v25
	v_mov_b32_e32 v74, v26
	v_mov_b32_e32 v75, v27
	v_mov_b32_e32 v76, v28
	v_mov_b32_e32 v77, v29
	v_mov_b32_e32 v78, v30
	v_mov_b32_e32 v79, v31
	v_mov_b32_e32 v80, v32
	v_mov_b32_e32 v81, v33
	v_mov_b32_e32 v82, v34
	v_mov_b32_e32 v83, v35
	v_mov_b32_e32 v84, v36
	v_mov_b32_e32 v85, v37
	v_mov_b32_e32 v86, v38
	v_mov_b32_e32 v87, v39
	v_mov_b32_e32 v88, v16
	v_mov_b32_e32 v89, v17
	v_mov_b32_e32 v90, v18
	v_mov_b32_e32 v91, v19
	v_mov_b32_e32 v92, v20
	v_mov_b32_e32 v93, v21
	v_mov_b32_e32 v94, v22
	v_mov_b32_e32 v95, v23
	v_mov_b32_e32 v96, v24
	v_mov_b32_e32 v97, v25
	v_mov_b32_e32 v98, v26
	v_mov_b32_e32 v99, v27
	v_mov_b32_e32 v100, v28
	v_mov_b32_e32 v101, v29
	v_mov_b32_e32 v102, v30
	v_mov_b32_e32 v103, v31
	v_mov_b32_e32 v104, v32
	v_mov_b32_e32 v105, v33
	v_mov_b32_e32 v106, v34
	v_mov_b32_e32 v107, v35
	v_mov_b32_e32 v108, v36
	v_mov_b32_e32 v109, v37
	v_mov_b32_e32 v110, v38
	v_mov_b32_e32 v111, v39
	v_mov_b32_e32 v112, v16
	v_mov_b32_e32 v113, v17
	v_mov_b32_e32 v114, v18
	v_mov_b32_e32 v115, v19
	v_mov_b32_e32 v116, v20
	v_mov_b32_e32 v117, v21
	v_mov_b32_e32 v118, v22
	v_mov_b32_e32 v119, v23
	v_mov_b32_e32 v120, v24
	v_mov_b32_e32 v121, v25
	v_mov_b32_e32 v122, v26
	v_mov_b32_e32 v123, v27
	v_mov_b32_e32 v124, v28
	v_mov_b32_e32 v125, v29
	v_mov_b32_e32 v126, v30
	v_mov_b32_e32 v127, v31
	v_mov_b32_e32 v128, v32
	v_mov_b32_e32 v129, v33
	v_mov_b32_e32 v130, v34
	v_mov_b32_e32 v131, v35
	v_mov_b32_e32 v132, v36
	v_mov_b32_e32 v133, v37
	v_mov_b32_e32 v134, v38
	v_mov_b32_e32 v135, v39
	v_mov_b32_e32 v136, v16
	v_mov_b32_e32 v137, v17
	v_mov_b32_e32 v138, v18
	v_mov_b32_e32 v139, v19
	v_mov_b32_e32 v140, v20
	v_mov_b32_e32 v141, v21
	v_mov_b32_e32 v142, v22
	v_mov_b32_e32 v143, v23
	v_mov_b32_e32 v144, v24
	v_mov_b32_e32 v145, v25
	v_mov_b32_e32 v146, v26
	v_mov_b32_e32 v147, v27
	v_mov_b32_e32 v148, v28
	v_mov_b32_e32 v149, v29
	v_mov_b32_e32 v150, v30
	v_mov_b32_e32 v151, v31
	v_mov_b32_e32 v152, v32
	v_mov_b32_e32 v153, v33
	v_mov_b32_e32 v154, v34
	v_mov_b32_e32 v155, v35
	v_mov_b32_e32 v156, v36
	v_mov_b32_e32 v157, v37
	v_mov_b32_e32 v158, v38
	v_mov_b32_e32 v159, v39
	v_mov_b32_e32 v160, v16
	v_mov_b32_e32 v161, v17
	v_mov_b32_e32 v162, v18
	v_mov_b32_e32 v163, v19
	v_mov_b32_e32 v164, v20
	v_mov_b32_e32 v165, v21
	v_mov_b32_e32 v166, v22
	v_mov_b32_e32 v167, v23
	v_mov_b32_e32 v168, v24
	v_mov_b32_e32 v169, v25
	v_mov_b32_e32 v170, v26
	v_mov_b32_e32 v171, v27
	v_mov_b32_e32 v172, v28
	v_mov_b32_e32 v173, v29
	v_mov_b32_e32 v174, v30
	v_mov_b32_e32 v175, v31
	v_mov_b32_e32 v176, v32
	v_mov_b32_e32 v177, v33
	v_mov_b32_e32 v178, v34
	v_mov_b32_e32 v179, v35
	v_mov_b32_e32 v180, v36
	v_mov_b32_e32 v181, v37
	v_mov_b32_e32 v182, v38
	v_mov_b32_e32 v183, v39
	v_mov_b32_e32 v184, v16
	v_mov_b32_e32 v185, v17
	v_mov_b32_e32 v186, v18
	v_mov_b32_e32 v187, v19
	v_mov_b32_e32 v188, v20
	v_mov_b32_e32 v189, v21
	v_mov_b32_e32 v190, v22
	v_mov_b32_e32 v191, v23
	v_mov_b32_e32 v192, v24
	v_mov_b32_e32 v193, v25
	v_mov_b32_e32 v194, v26
	v_mov_b32_e32 v195, v27
	v_mov_b32_e32 v196, v28
	v_mov_b32_e32 v197, v29
	v_mov_b32_e32 v198, v30
	v_mov_b32_e32 v199, v31
	v_mov_b32_e32 v200, v32
	v_mov_b32_e32 v201, v33
	v_mov_b32_e32 v202, v34
	v_mov_b32_e32 v203, v35
	v_mov_b32_e32 v204, v36
	v_mov_b32_e32 v205, v37
	v_mov_b32_e32 v206, v38
	v_mov_b32_e32 v207, v39
	v_mov_b32_e32 v208, v16
	v_mov_b32_e32 v209, v17
	v_mov_b32_e32 v210, v18
	v_mov_b32_e32 v211, v19
	v_mov_b32_e32 v212, v20
	v_mov_b32_e32 v213, v21
	v_mov_b32_e32 v214, v22
	v_mov_b32_e32 v215, v23
	v_mov_b32_e32 v216, v24
	v_mov_b32_e32 v217, v25
	v_mov_b32_e32 v218, v26
	v_mov_b32_e32 v219, v27
	v_mov_b32_e32 v220, v28
	v_mov_b32_e32 v221, v29
	v_mov_b32_e32 v222, v30
	v_mov_b32_e32 v223, v31
	v_mov_b32_e32 v224, v32
	v_mov_b32_e32 v225, v33
	v_mov_b32_e32 v226, v34
	v_mov_b32_e32 v227, v35
	v_mov_b32_e32 v228, v36
	v_mov_b32_e32 v229, v37
	v_mov_b32_e32 v230, v38
	v_mov_b32_e32 v231, v39
	v_mov_b32_e32 v232, v16
	v_mov_b32_e32 v233, v17
	v_mov_b32_e32 v234, v18
	v_mov_b32_e32 v235, v19
	v_mov_b32_e32 v236, v20
	v_mov_b32_e32 v237, v21
	v_mov_b32_e32 v238, v22
	v_mov_b32_e32 v239, v23
	v_mov_b32_e32 v240, v24
	v_mov_b32_e32 v241, v25
	v_mov_b32_e32 v242, v26
	v_mov_b32_e32 v243, v27
	v_mov_b32_e32 v244, v28
	v_mov_b32_e32 v245, v29
	v_mov_b32_e32 v246, v30
	v_mov_b32_e32 v247, v31
	v_mov_b32_e32 v248, v32
	v_mov_b32_e32 v249, v33
	v_mov_b32_e32 v250, v34
	v_mov_b32_e32 v251, v35
	v_mov_b32_e32 v252, v36
	v_mov_b32_e32 v253, v37
	v_mov_b32_e32 v254, v38
	v_mov_b32_e32 v255, v39
	s_waitcnt vmcnt(10)
	s_barrier
	s_barrier
.Lfc_h1_loop:
	ds_read_b128 v[16:19], v3 offset:0
	ds_read_b128 v[20:23], v3 offset:1024
	ds_read_b128 v[24:27], v3 offset:2048
	ds_read_b128 v[28:31], v3 offset:3072
	ds_read_b128 v[32:35], v3 offset:4096
	ds_read_b128 v[36:39], v3 offset:5120
	ds_read_b128 v[40:43], v1 offset:0
	ds_read_b128 v[44:47], v1 offset:1024
	ds_read_b128 v[48:51], v1 offset:2048
	ds_read_b128 v[52:55], v1 offset:3072
	s_add_u32 m0, s22, 0x1e000
	s_nop 0
	global_load_lds_dwordx4 v5, s[26:27]
	s_add_u32 m0, s22, 0x1e400
	s_nop 0
	global_load_lds_dwordx4 v6, s[26:27]
	s_add_u32 m0, s23, 0x1e000
	s_nop 0
	global_load_lds_dwordx4 v11, s[30:31]
	s_add_u32 m0, s23, 0x1e400
	s_nop 0
	global_load_lds_dwordx4 v11, s[34:35]
	s_add_u32 m0, s23, 0x1e800
	s_nop 0
	global_load_lds_dwordx4 v11, s[38:39]
	s_add_u32 s26, s26, 0x80
	s_addc_u32 s27, s27, 0
	s_add_u32 s30, s30, 0x30000
	s_addc_u32 s31, s31, 0
	s_add_u32 s34, s34, 0x30000
	s_addc_u32 s35, s35, 0
	s_add_u32 s38, s38, 0x30000
	s_addc_u32 s39, s39, 0
	s_cmp_eq_u32 s21, 3
	s_cbranch_scc1 .Lfc_sw_8
	s_cmp_eq_u32 s21, 7
	s_cbranch_scc0 .Lfc_swd_8
	s_add_u32 s28, s28, 0x180000
	s_addc_u32 s29, s29, 0
	s_add_u32 s30, s30, 0x180000
	s_addc_u32 s31, s31, 0
	s_add_u32 s32, s32, 0x180000
	s_addc_u32 s33, s33, 0
	s_add_u32 s34, s34, 0x180000
	s_addc_u32 s35, s35, 0
	s_add_u32 s36, s36, 0x180000
	s_addc_u32 s37, s37, 0
	s_add_u32 s38, s38, 0x180000
	s_addc_u32 s39, s39, 0
	s_branch .Lfc_sw2_8

.Lfc_sw2_8:
	s_mov_b64 s[24:25], s[4:5]
	s_add_u32 s26, s4, 0x40
	s_addc_u32 s27, s5, 0
	v_mov_b32_e32 v5, v7
	v_mov_b32_e32 v6, v8
	v_mov_b32_e32 v7, v9
	v_mov_b32_e32 v8, v10
.Lfc_swd_8:
	s_cmp_eq_u32 s21, 11
	s_cbranch_scc1 .Lfc_w0_9
	s_waitcnt vmcnt(10)
	s_branch .Lfc_w1_9
